# v39 with k_main .sgpr_count metadata made truthful (105); same code
# speedup vs baseline: 1.0094x; 1.0094x over previous
amdhsa.kernels:
  - .agpr_count:     0
    .args:
      - .actual_access:  read_only
        .address_space:  global
        .offset:         0
        .size:           8
        .value_kind:     global_buffer
      - .actual_access:  read_only
        .address_space:  global
        .offset:         8
        .size:           8
        .value_kind:     global_buffer
      - .actual_access:  read_only
        .address_space:  global
        .offset:         16
        .size:           8
        .value_kind:     global_buffer
      - .actual_access:  read_only
        .address_space:  global
        .offset:         24
        .size:           8
        .value_kind:     global_buffer
      - .actual_access:  read_only
        .address_space:  global
        .offset:         32
        .size:           8
        .value_kind:     global_buffer
      - .actual_access:  write_only
        .address_space:  global
        .offset:         40
        .size:           8
        .value_kind:     global_buffer
      - .actual_access:  write_only
        .address_space:  global
        .offset:         48
        .size:           8
        .value_kind:     global_buffer
      - .actual_access:  write_only
        .address_space:  global
        .offset:         56
        .size:           8
        .value_kind:     global_buffer
      - .actual_access:  write_only
        .address_space:  global
        .offset:         64
        .size:           8
        .value_kind:     global_buffer
      - .actual_access:  write_only
        .address_space:  global
        .offset:         72
        .size:           8
        .value_kind:     global_buffer
      - .actual_access:  write_only
        .address_space:  global
        .offset:         80
        .size:           8
        .value_kind:     global_buffer
      - .actual_access:  write_only
        .address_space:  global
        .offset:         88
        .size:           8
        .value_kind:     global_buffer
      - .actual_access:  write_only
        .address_space:  global
        .offset:         96
        .size:           8
        .value_kind:     global_buffer
    .group_segment_fixed_size: 73760
    .kernarg_segment_align: 8
    .kernarg_segment_size: 104
    .language:       OpenCL C
    .language_version:
      - 2
      - 0
    .max_flat_workgroup_size: 512
    .name:           _Z6k_prepPKfS0_S0_S0_S0_PfPDF16_S1_S1_S1_S1_S1_Pi
    .private_segment_fixed_size: 0
    .sgpr_count:     35
    .sgpr_spill_count: 0
    .symbol:         _Z6k_prepPKfS0_S0_S0_S0_PfPDF16_S1_S1_S1_S1_S1_Pi.kd
    .uniform_work_group_size: 1
    .uses_dynamic_stack: false
    .vgpr_count:     127
    .vgpr_spill_count: 0
    .wavefront_size: 64
  - .agpr_count:     0
    .args:
      - .actual_access:  read_only
        .address_space:  global
        .offset:         0
        .size:           8
        .value_kind:     global_buffer
      - .actual_access:  read_only
        .address_space:  global
        .offset:         8
        .size:           8
        .value_kind:     global_buffer
      - .actual_access:  read_only
        .address_space:  global
        .offset:         16
        .size:           8
        .value_kind:     global_buffer
      - .address_space:  global
        .offset:         24
        .size:           8
        .value_kind:     global_buffer
      - .actual_access:  read_only
        .address_space:  global
        .offset:         32
        .size:           8
        .value_kind:     global_buffer
      - .actual_access:  read_only
        .address_space:  global
        .offset:         40
        .size:           8
        .value_kind:     global_buffer
      - .actual_access:  read_only
        .address_space:  global
        .offset:         48
        .size:           8
        .value_kind:     global_buffer
      - .actual_access:  read_only
        .address_space:  global
        .offset:         56
        .size:           8
        .value_kind:     global_buffer
      - .actual_access:  read_only
        .address_space:  global
        .offset:         64
        .size:           8
        .value_kind:     global_buffer
      - .actual_access:  read_only
        .address_space:  global
        .offset:         72
        .size:           8
        .value_kind:     global_buffer
      - .actual_access:  write_only
        .address_space:  global
        .offset:         80
        .size:           8
        .value_kind:     global_buffer
      - .actual_access:  write_only
        .address_space:  global
        .offset:         88
        .size:           8
        .value_kind:     global_buffer
      - .address_space:  global
        .offset:         96
        .size:           8
        .value_kind:     global_buffer
      - .actual_access:  write_only
        .address_space:  global
        .offset:         104
        .size:           8
        .value_kind:     global_buffer
    .group_segment_fixed_size: 105056
    .kernarg_segment_align: 8
    .kernarg_segment_size: 112
    .language:       OpenCL C
    .language_version:
      - 2
      - 0
    .max_flat_workgroup_size: 512
    .name:           _Z6k_mainPKfS0_S0_PKDF16_S0_S0_S0_S0_S0_S0_PfP15HIP_vector_typeIiLj4EEPiS3_
    .private_segment_fixed_size: 0
    .sgpr_count:     105
    .sgpr_spill_count: 0
    .symbol:         _Z6k_mainPKfS0_S0_PKDF16_S0_S0_S0_S0_S0_S0_PfP15HIP_vector_typeIiLj4EEPiS3_.kd
    .uniform_work_group_size: 1
    .uses_dynamic_stack: false
    .vgpr_count:     248
    .vgpr_spill_count: 0
    .wavefront_size: 64
  - .agpr_count:     0
    .args:
      - .actual_access:  read_only
        .address_space:  global
        .offset:         0
        .size:           8
        .value_kind:     global_buffer
      - .actual_access:  read_only
        .address_space:  global
        .offset:         8
        .size:           8
        .value_kind:     global_buffer
      - .actual_access:  read_only
        .address_space:  global
        .offset:         16
        .size:           8
        .value_kind:     global_buffer
      - .actual_access:  read_only
        .address_space:  global
        .offset:         24
        .size:           8
        .value_kind:     global_buffer
      - .actual_access:  read_only
        .address_space:  global
        .offset:         32
        .size:           8
        .value_kind:     global_buffer
      - .actual_access:  read_only
        .address_space:  global
        .offset:         40
        .size:           8
        .value_kind:     global_buffer
      - .actual_access:  read_only
        .address_space:  global
        .offset:         48
        .size:           8
        .value_kind:     global_buffer
      - .actual_access:  read_only
        .address_space:  global
        .offset:         56
        .size:           8
        .value_kind:     global_buffer
      - .address_space:  global
        .offset:         64
        .size:           8
        .value_kind:     global_buffer
      - .address_space:  global
        .offset:         72
        .size:           8
        .value_kind:     global_buffer
      - .actual_access:  read_only
        .address_space:  global
        .offset:         80
        .size:           8
        .value_kind:     global_buffer
      - .actual_access:  read_only
        .address_space:  global
        .offset:         88
        .size:           8
        .value_kind:     global_buffer
      - .actual_access:  write_only
        .address_space:  global
        .offset:         96
        .size:           8
        .value_kind:     global_buffer
      - .offset:         104
        .size:           4
        .value_kind:     hidden_block_count_x
      - .offset:         108
        .size:           4
        .value_kind:     hidden_block_count_y
      - .offset:         112
        .size:           4
        .value_kind:     hidden_block_count_z
      - .offset:         116
        .size:           2
        .value_kind:     hidden_group_size_x
      - .offset:         118
        .size:           2
        .value_kind:     hidden_group_size_y
      - .offset:         120
        .size:           2
        .value_kind:     hidden_group_size_z
      - .offset:         122
        .size:           2
        .value_kind:     hidden_remainder_x
      - .offset:         124
        .size:           2
        .value_kind:     hidden_remainder_y
      - .offset:         126
        .size:           2
        .value_kind:     hidden_remainder_z
      - .offset:         144
        .size:           8
        .value_kind:     hidden_global_offset_x
      - .offset:         152
        .size:           8
        .value_kind:     hidden_global_offset_y
      - .offset:         160
        .size:           8
        .value_kind:     hidden_global_offset_z
      - .offset:         168
        .size:           2
        .value_kind:     hidden_grid_dims
    .group_segment_fixed_size: 4120
    .kernarg_segment_align: 8
    .kernarg_segment_size: 360
    .language:       OpenCL C
    .language_version:
      - 2
      - 0
    .max_flat_workgroup_size: 256
    .name:           _Z4k_t2PKfS0_S0_S0_S0_S0_PK15HIP_vector_typeIiLj4EEPKiPdPiS0_S0_Pf
    .private_segment_fixed_size: 0
    .sgpr_count:     106
    .sgpr_spill_count: 0
    .symbol:         _Z4k_t2PKfS0_S0_S0_S0_S0_PK15HIP_vector_typeIiLj4EEPKiPdPiS0_S0_Pf.kd
    .uniform_work_group_size: 1
    .uses_dynamic_stack: false
    .vgpr_count:     158
    .vgpr_spill_count: 0
    .wavefront_size: 64
